# GEMM-in: stage waits split by consumer (vmcnt 10/8), tail scalar work moved into the MFMA shadow; E: segment constants issued before the first-row wait; GDN compute waves at default priority
# speedup vs baseline: 1.0012x; 1.0012x over previous
; #define LDS_BARRIER() asm volatile("s_waitcnt lgkmcnt(0)\n\ts_barrier" ::: "memory")
; __device__ void phase_gdn_chain(const Params& p, int l, char* smem, int vb, int nvb, int oz) {
;     ...
;     for (int it = vb; it < 64; it += nvb) {
;         const int b = it >> 3, h = (it >> 1) & 3, dir = it & 1;
;     ...
;         if (loader) {
;     ...
;         } else {
;             f32x4 S[4];
; #pragma unroll
;             for (int mt = 0; mt < 4; ++mt) S[mt] = (f32x4){0.f, 0.f, 0.f, 0.f};
;             bf16x4 ost[4], onew[4];
; #pragma unroll
;             for (int mt = 0; mt < 4; ++mt) { ost[mt] = (bf16x4){0, 0, 0, 0}; onew[mt] = (bf16x4){0, 0, 0, 0}; }
;             size_t orow = 0;
;             bool ohave = false;
;             if (__builtin_amdgcn_readfirstlane(wave) < 4) __builtin_amdgcn_s_setprio(3);
;             LDS_BARRIER();
.LBB0_390:
	s_ashr_i32 s46, s93, 3
	s_bfe_u32 s2, s93, 0x20001
	s_and_saveexec_b64 s[0:1], s[36:37]
	s_xor_b64 s[48:49], exec, s[0:1]
	s_cbranch_execz .LBB0_418
	v_readfirstlane_b32 s0, v1
	s_cmp_gt_i32 s0, 3
	s_cbranch_scc1 .LBB0_393
	s_setprio 0

; #define G8_STAGE(bufoff, gbase, voff) do { _Pragma("unroll") for (int _i = 0; _i < 2; ++_i) \
;         __builtin_amdgcn_global_load_lds((const unsigned*)((const char*)(gbase) + (voff)[_i]), (G8_LAS unsigned*)(lds + (bufoff) + ldsw + _i * 8192), 16, 0, 0); } while (0)
; #define G8_LDA(dst, b, h) do { _Pragma("unroll") for (int m = 0; m < 4; ++m) _Pragma("unroll") for (int k = 0; k < 2; ++k) dst[m][k] = *(const G8_LAS bf16x8*)(lds + G8_SA(b, h) + aoff + m * 2048 + k * 1024); } while (0)
; #define G8_LDB(dst, b, h) do { _Pragma("unroll") for (int n = 0; n < 2; ++n) _Pragma("unroll") for (int k = 0; k < 2; ++k) dst[n][k] = *(const G8_LAS bf16x8*)(lds + G8_SB(b, h) + boff + n * 2048 + k * 1024); } while (0)
; #define G8_MMA(ai, bj, At, Bt) do { __builtin_amdgcn_s_setprio(1); _Pragma("unroll") for (int m = 0; m < 4; ++m) _Pragma("unroll") for (int n = 0; n < 2; ++n) _Pragma("unroll") for (int k = 0; k < 2; ++k) \
;         acc[ai][bj][m][n] = __builtin_amdgcn_mfma_f32_16x16x32_bf16(Bt[n][k], At[m][k], acc[ai][bj][m][n], 0, 0, 0); __builtin_amdgcn_s_setprio(0); } while (0)
; #define G8_WAIT_L(n) asm volatile("s_waitcnt lgkmcnt(" #n ")" ::: "memory")
; #define G8_BAR __builtin_amdgcn_s_barrier()
; #define G8_SCHED __builtin_amdgcn_sched_barrier(0)
; template <bool OUTP>
; __device__ __forceinline__ void gemm_phase(const Params& p, int l, char* smem, int vb, int nvb, int pm0, int M, bool fuse, int oz) {
;     ...
;             G8_LDB(B0, 0, 0); G8_SCHED; G8_LDA(At, 0, 0); G8_STAGE(G8_SA(1, 1), a1 + hstepA, voffA);
;             G8_WAIT_L(8); G8_BAR; G8_WAIT_L(0); G8_MMA(0, 0, At, B0); G8_BAR; G8_SCHED;
;             G8_LDB(B1, 0, 1); G8_STAGE(G8_SB(0, 0), b2, voffB);
;             G8_BAR; G8_WAIT_L(0); G8_MMA(0, 1, At, B1); G8_BAR;
;             G8_LDA(At, 0, 1); G8_STAGE(G8_SA(0, 0), a2, voffA);
;             G8_BAR; G8_WAIT_L(0); G8_MMA(1, 0, At, B0); G8_BAR; G8_SCHED;
.LBB0_746:
	s_add_u32 s46, s38, 0xfffc0080
	s_addc_u32 s47, s39, -1
	s_add_i32 s56, 0, 0x10000
	v_add_u32_e32 v146, s56, v148
	ds_read_b128 v[142:145], v146
	ds_read_b128 v[152:155], v146 offset:1024
	ds_read_b128 v[156:159], v146 offset:2048
	ds_read_b128 v[160:163], v146 offset:3072
	s_cmp_eq_u32 s55, 12
	s_cselect_b32 s49, s1, s47
	s_cselect_b32 s48, s41, s46
	s_cselect_b32 s47, s29, s54
	s_cselect_b32 s46, s52, s53
	v_lshl_add_u64 v[146:147], s[38:39], 0, v[138:139]
	s_add_i32 m0, s21, 0xc000
	ds_read_b128 v[164:167], v150
	ds_read_b128 v[168:171], v150 offset:1024
	ds_read_b128 v[172:175], v150 offset:2048
	ds_read_b128 v[176:179], v150 offset:3072
	ds_read_b128 v[180:183], v150 offset:4096
	ds_read_b128 v[184:187], v150 offset:5120
	ds_read_b128 v[188:191], v150 offset:6144
	ds_read_b128 v[192:195], v150 offset:7168
	global_load_lds_dwordx4 v[146:147], off
	v_lshl_add_u64 v[146:147], s[38:39], 0, v[140:141]
	s_add_i32 m0, s21, 0xe000
	s_nop 0
	global_load_lds_dwordx4 v[146:147], off
	s_waitcnt lgkmcnt(8)
	s_barrier
	s_waitcnt lgkmcnt(0)
	s_setprio 1
	s_waitcnt lgkmcnt(0)
	v_mfma_f32_16x16x32_bf16 v[128:131], v[142:145], v[164:167], v[128:131]
	v_mfma_f32_16x16x32_bf16 v[124:127], v[156:159], v[164:167], v[124:127]
	v_mfma_f32_16x16x32_bf16 v[120:123], v[142:145], v[172:175], v[120:123]
	v_mfma_f32_16x16x32_bf16 v[112:115], v[156:159], v[172:175], v[112:115]
	v_mfma_f32_16x16x32_bf16 v[104:107], v[142:145], v[180:183], v[104:107]
	v_mfma_f32_16x16x32_bf16 v[96:99], v[156:159], v[180:183], v[96:99]
	v_mfma_f32_16x16x32_bf16 v[88:91], v[142:145], v[188:191], v[88:91]
	v_mfma_f32_16x16x32_bf16 v[80:83], v[156:159], v[188:191], v[80:83]
	v_mfma_f32_16x16x32_bf16 v[128:131], v[152:155], v[168:171], v[128:131]
	v_mfma_f32_16x16x32_bf16 v[124:127], v[160:163], v[168:171], v[124:127]
	v_mfma_f32_16x16x32_bf16 v[120:123], v[152:155], v[176:179], v[120:123]
	v_mfma_f32_16x16x32_bf16 v[112:115], v[160:163], v[176:179], v[112:115]
	v_mfma_f32_16x16x32_bf16 v[104:107], v[152:155], v[184:187], v[104:107]
	v_mfma_f32_16x16x32_bf16 v[96:99], v[160:163], v[184:187], v[96:99]
	v_mfma_f32_16x16x32_bf16 v[88:91], v[152:155], v[192:195], v[88:91]
	v_mfma_f32_16x16x32_bf16 v[80:83], v[160:163], v[192:195], v[80:83]
	s_setprio 0
	s_barrier
	s_add_i32 s58, 0, 0x14000
	v_add_u32_e32 v146, s58, v148
	s_add_i32 s56, s56, s3
	ds_read_b128 v[202:205], v146
	ds_read_b128 v[206:209], v146 offset:1024
	ds_read_b128 v[210:213], v146 offset:2048
	ds_read_b128 v[214:217], v146 offset:3072
	v_lshl_add_u64 v[146:147], s[46:47], 0, v[2:3]
	s_mov_b32 m0, s56
	v_lshl_add_u64 v[218:219], s[46:47], 0, v[136:137]
	global_load_lds_dwordx4 v[146:147], off
	s_add_i32 m0, s56, 0x2000
	s_nop 0
	global_load_lds_dwordx4 v[218:219], off
	s_waitcnt vmcnt(10)
	s_barrier
	s_waitcnt lgkmcnt(0)
	s_setprio 1
	s_waitcnt lgkmcnt(0)
	v_mfma_f32_16x16x32_bf16 v[116:119], v[202:205], v[164:167], v[116:119]
	v_mfma_f32_16x16x32_bf16 v[108:111], v[210:213], v[164:167], v[108:111]
	v_mfma_f32_16x16x32_bf16 v[100:103], v[202:205], v[172:175], v[100:103]
	v_mfma_f32_16x16x32_bf16 v[92:95], v[210:213], v[172:175], v[92:95]
	v_mfma_f32_16x16x32_bf16 v[84:87], v[202:205], v[180:183], v[84:87]
	v_mfma_f32_16x16x32_bf16 v[76:79], v[210:213], v[180:183], v[76:79]
	v_mfma_f32_16x16x32_bf16 v[72:75], v[202:205], v[188:191], v[72:75]
	v_mfma_f32_16x16x32_bf16 v[68:71], v[210:213], v[188:191], v[68:71]
	s_mov_b32 m0, s21
	v_lshl_add_u64 v[220:221], s[48:49], 0, v[132:133]
	v_mfma_f32_16x16x32_bf16 v[116:119], v[206:209], v[168:171], v[116:119]
	v_mfma_f32_16x16x32_bf16 v[108:111], v[214:217], v[168:171], v[108:111]
	v_mfma_f32_16x16x32_bf16 v[100:103], v[206:209], v[176:179], v[100:103]
	v_mfma_f32_16x16x32_bf16 v[92:95], v[214:217], v[176:179], v[92:95]
	v_mfma_f32_16x16x32_bf16 v[84:87], v[206:209], v[184:187], v[84:87]
	v_mfma_f32_16x16x32_bf16 v[76:79], v[214:217], v[184:187], v[76:79]
	v_mfma_f32_16x16x32_bf16 v[72:75], v[206:209], v[192:195], v[72:75]
	v_mfma_f32_16x16x32_bf16 v[68:71], v[214:217], v[192:195], v[68:71]
	s_setprio 0
	s_barrier
	ds_read_b128 v[164:167], v150 offset:16384
	ds_read_b128 v[168:171], v150 offset:17408
	ds_read_b128 v[172:175], v150 offset:18432
	ds_read_b128 v[176:179], v150 offset:19456
	ds_read_b128 v[180:183], v150 offset:20480
	ds_read_b128 v[184:187], v150 offset:21504
	ds_read_b128 v[188:191], v150 offset:22528
	ds_read_b128 v[192:195], v150 offset:23552
	global_load_lds_dwordx4 v[220:221], off
	v_lshl_add_u64 v[222:223], s[48:49], 0, v[134:135]
	s_mov_b32 m0, s24
	s_nop 0
	global_load_lds_dwordx4 v[222:223], off
	s_barrier
	s_waitcnt lgkmcnt(0)
	s_setprio 1
	s_waitcnt lgkmcnt(0)
	v_mfma_f32_16x16x32_bf16 v[64:67], v[142:145], v[164:167], v[64:67]
	v_mfma_f32_16x16x32_bf16 v[60:63], v[156:159], v[164:167], v[60:63]
	v_mfma_f32_16x16x32_bf16 v[56:59], v[142:145], v[172:175], v[56:59]
	v_mfma_f32_16x16x32_bf16 v[48:51], v[156:159], v[172:175], v[48:51]
	v_mfma_f32_16x16x32_bf16 v[40:43], v[142:145], v[180:183], v[40:43]
	v_mfma_f32_16x16x32_bf16 v[32:35], v[156:159], v[180:183], v[32:35]
	v_mfma_f32_16x16x32_bf16 v[24:27], v[142:145], v[188:191], v[24:27]
	v_mfma_f32_16x16x32_bf16 v[16:19], v[156:159], v[188:191], v[16:19]
	v_mfma_f32_16x16x32_bf16 v[64:67], v[152:155], v[168:171], v[64:67]
	v_mfma_f32_16x16x32_bf16 v[60:63], v[160:163], v[168:171], v[60:63]
	v_mfma_f32_16x16x32_bf16 v[56:59], v[152:155], v[176:179], v[56:59]
	v_mfma_f32_16x16x32_bf16 v[48:51], v[160:163], v[176:179], v[48:51]
	v_mfma_f32_16x16x32_bf16 v[40:43], v[152:155], v[184:187], v[40:43]
	v_mfma_f32_16x16x32_bf16 v[32:35], v[160:163], v[184:187], v[32:35]
	v_mfma_f32_16x16x32_bf16 v[24:27], v[152:155], v[192:195], v[24:27]
	v_mfma_f32_16x16x32_bf16 v[16:19], v[160:163], v[192:195], v[16:19]
	s_setprio 0
	s_barrier
; #define G8_STAGE(bufoff, gbase, voff) do { _Pragma("unroll") for (int _i = 0; _i < 2; ++_i) \
;         __builtin_amdgcn_global_load_lds((const unsigned*)((const char*)(gbase) + (voff)[_i]), (G8_LAS unsigned*)(lds + (bufoff) + ldsw + _i * 8192), 16, 0, 0); } while (0)
; #define G8_LDA(dst, b, h) do { _Pragma("unroll") for (int m = 0; m < 4; ++m) _Pragma("unroll") for (int k = 0; k < 2; ++k) dst[m][k] = *(const G8_LAS bf16x8*)(lds + G8_SA(b, h) + aoff + m * 2048 + k * 1024); } while (0)
; #define G8_LDB(dst, b, h) do { _Pragma("unroll") for (int n = 0; n < 2; ++n) _Pragma("unroll") for (int k = 0; k < 2; ++k) dst[n][k] = *(const G8_LAS bf16x8*)(lds + G8_SB(b, h) + boff + n * 2048 + k * 1024); } while (0)
; #define G8_MMA(ai, bj, At, Bt) do { __builtin_amdgcn_s_setprio(1); _Pragma("unroll") for (int m = 0; m < 4; ++m) _Pragma("unroll") for (int n = 0; n < 2; ++n) _Pragma("unroll") for (int k = 0; k < 2; ++k) \
;         acc[ai][bj][m][n] = __builtin_amdgcn_mfma_f32_16x16x32_bf16(Bt[n][k], At[m][k], acc[ai][bj][m][n], 0, 0, 0); __builtin_amdgcn_s_setprio(0); } while (0)
; #define G8_WAIT_V(n) asm volatile("s_waitcnt vmcnt(" #n ")" ::: "memory")
; #define G8_WAIT_L(n) asm volatile("s_waitcnt lgkmcnt(" #n ")" ::: "memory")
; #define G8_BAR __builtin_amdgcn_s_barrier()
; #define G8_SCHED __builtin_amdgcn_sched_barrier(0)
; template <bool OUTP>
; __device__ __forceinline__ void gemm_phase(const Params& p, int l, char* smem, int vb, int nvb, int pm0, int M, bool fuse, int oz) {
;     ...
;             G8_STAGE(G8_SB(0, 1), b2 + hstepB, voffB);
;             G8_WAIT_V(6); G8_BAR; G8_MMA(1, 1, At, B1); G8_BAR;
;             G8_LDB(B0, 1, 0); G8_SCHED; G8_LDA(At, 1, 0); G8_STAGE(G8_SA(0, 1), a2 + hstepA, voffA);
;             G8_WAIT_L(8); G8_BAR; G8_WAIT_L(0); G8_MMA(0, 0, At, B0); G8_BAR; G8_SCHED;
;             G8_LDB(B1, 1, 1); G8_STAGE(G8_SB(1, 0), b3, voffB);
;             G8_BAR; G8_WAIT_L(0); G8_MMA(0, 1, At, B1); G8_BAR;
	s_add_u32 s56, s46, 0x40000
	s_addc_u32 s57, s47, 0
	s_add_i32 s58, s58, s3
	v_lshl_add_u64 v[142:143], s[56:57], 0, v[2:3]
	s_mov_b32 m0, s58
	s_nop 0
	global_load_lds_dwordx4 v[142:143], off
	v_lshl_add_u64 v[142:143], s[56:57], 0, v[136:137]
	s_add_i32 m0, s58, 0x2000
	s_nop 0
	global_load_lds_dwordx4 v[142:143], off
	s_waitcnt vmcnt(8)
	s_barrier
	s_setprio 1
	v_mfma_f32_16x16x32_bf16 v[52:55], v[202:205], v[164:167], v[52:55]
	v_mfma_f32_16x16x32_bf16 v[44:47], v[210:213], v[164:167], v[44:47]
	v_mfma_f32_16x16x32_bf16 v[36:39], v[202:205], v[172:175], v[36:39]
	v_mfma_f32_16x16x32_bf16 v[28:31], v[210:213], v[172:175], v[28:31]
	v_mfma_f32_16x16x32_bf16 v[20:23], v[202:205], v[180:183], v[20:23]
	v_mfma_f32_16x16x32_bf16 v[12:15], v[210:213], v[180:183], v[12:15]
	v_mfma_f32_16x16x32_bf16 v[8:11], v[202:205], v[188:191], v[8:11]
	v_mfma_f32_16x16x32_bf16 v[4:7], v[210:213], v[188:191], v[4:7]
	s_add_i32 s56, 0, 0x18000
	v_add_u32_e32 v151, s56, v148
	v_mfma_f32_16x16x32_bf16 v[52:55], v[206:209], v[168:171], v[52:55]
	v_mfma_f32_16x16x32_bf16 v[44:47], v[214:217], v[168:171], v[44:47]
	v_mfma_f32_16x16x32_bf16 v[36:39], v[206:209], v[176:179], v[36:39]
	v_mfma_f32_16x16x32_bf16 v[28:31], v[214:217], v[176:179], v[28:31]
	v_mfma_f32_16x16x32_bf16 v[20:23], v[206:209], v[184:187], v[20:23]
	v_mfma_f32_16x16x32_bf16 v[12:15], v[214:217], v[184:187], v[12:15]
	v_mfma_f32_16x16x32_bf16 v[8:11], v[206:209], v[192:195], v[8:11]
	v_mfma_f32_16x16x32_bf16 v[4:7], v[214:217], v[192:195], v[4:7]
	s_setprio 0
	s_barrier
	ds_read_b128 v[142:145], v151
	ds_read_b128 v[152:155], v151 offset:1024
	ds_read_b128 v[156:159], v151 offset:2048
	ds_read_b128 v[160:163], v151 offset:3072
	s_add_u32 s48, s48, 0x40000
	s_addc_u32 s49, s49, 0
	s_mov_b32 m0, s25
	v_lshl_add_u64 v[202:203], s[48:49], 0, v[132:133]
	ds_read_b128 v[164:167], v150 offset:32768
	ds_read_b128 v[168:171], v150 offset:33792
	ds_read_b128 v[172:175], v150 offset:34816
	ds_read_b128 v[176:179], v150 offset:35840
	ds_read_b128 v[180:183], v150 offset:36864
	ds_read_b128 v[184:187], v150 offset:37888
	ds_read_b128 v[188:191], v150 offset:38912
	ds_read_b128 v[192:195], v150 offset:39936
	global_load_lds_dwordx4 v[202:203], off
	v_lshl_add_u64 v[202:203], s[48:49], 0, v[134:135]
	s_mov_b32 m0, s26
	s_nop 0
	global_load_lds_dwordx4 v[202:203], off
	s_waitcnt lgkmcnt(8)
	s_barrier
	s_waitcnt lgkmcnt(0)
	s_setprio 1
	s_waitcnt lgkmcnt(0)
	v_mfma_f32_16x16x32_bf16 v[128:131], v[142:145], v[164:167], v[128:131]
	v_mfma_f32_16x16x32_bf16 v[124:127], v[156:159], v[164:167], v[124:127]
	v_mfma_f32_16x16x32_bf16 v[120:123], v[142:145], v[172:175], v[120:123]
	v_mfma_f32_16x16x32_bf16 v[112:115], v[156:159], v[172:175], v[112:115]
	v_mfma_f32_16x16x32_bf16 v[104:107], v[142:145], v[180:183], v[104:107]
	v_mfma_f32_16x16x32_bf16 v[96:99], v[156:159], v[180:183], v[96:99]
	v_mfma_f32_16x16x32_bf16 v[88:91], v[142:145], v[188:191], v[88:91]
	v_mfma_f32_16x16x32_bf16 v[80:83], v[156:159], v[188:191], v[80:83]
	v_mfma_f32_16x16x32_bf16 v[128:131], v[152:155], v[168:171], v[128:131]
	v_mfma_f32_16x16x32_bf16 v[124:127], v[160:163], v[168:171], v[124:127]
	v_mfma_f32_16x16x32_bf16 v[120:123], v[152:155], v[176:179], v[120:123]
	v_mfma_f32_16x16x32_bf16 v[112:115], v[160:163], v[176:179], v[112:115]
	v_mfma_f32_16x16x32_bf16 v[104:107], v[152:155], v[184:187], v[104:107]
	v_mfma_f32_16x16x32_bf16 v[96:99], v[160:163], v[184:187], v[96:99]
	v_mfma_f32_16x16x32_bf16 v[88:91], v[152:155], v[192:195], v[88:91]
	v_mfma_f32_16x16x32_bf16 v[80:83], v[160:163], v[192:195], v[80:83]
	s_setprio 0
	s_barrier
	s_add_i32 s48, 0, 0x1c000
	s_add_i32 s49, s56, s3
	v_add_u32_e32 v151, s48, v148
	v_lshl_add_u64 v[146:147], v[146:147], 0, s[90:91]
	s_mov_b32 m0, s49
	ds_read_b128 v[202:205], v151
	ds_read_b128 v[206:209], v151 offset:1024
	ds_read_b128 v[210:213], v151 offset:2048
	ds_read_b128 v[214:217], v151 offset:3072
	global_load_lds_dwordx4 v[146:147], off
	v_lshl_add_u64 v[146:147], v[218:219], 0, s[90:91]
	s_add_i32 m0, s49, 0x2000
	s_nop 0
	global_load_lds_dwordx4 v[146:147], off
	s_waitcnt vmcnt(10)
	s_barrier
; #define G8_STAGE(bufoff, gbase, voff) do { _Pragma("unroll") for (int _i = 0; _i < 2; ++_i) \
;         __builtin_amdgcn_global_load_lds((const unsigned*)((const char*)(gbase) + (voff)[_i]), (G8_LAS unsigned*)(lds + (bufoff) + ldsw + _i * 8192), 16, 0, 0); } while (0)
; #define G8_LDA(dst, b, h) do { _Pragma("unroll") for (int m = 0; m < 4; ++m) _Pragma("unroll") for (int k = 0; k < 2; ++k) dst[m][k] = *(const G8_LAS bf16x8*)(lds + G8_SA(b, h) + aoff + m * 2048 + k * 1024); } while (0)
; #define G8_MMA(ai, bj, At, Bt) do { __builtin_amdgcn_s_setprio(1); _Pragma("unroll") for (int m = 0; m < 4; ++m) _Pragma("unroll") for (int n = 0; n < 2; ++n) _Pragma("unroll") for (int k = 0; k < 2; ++k) \
;         acc[ai][bj][m][n] = __builtin_amdgcn_mfma_f32_16x16x32_bf16(Bt[n][k], At[m][k], acc[ai][bj][m][n], 0, 0, 0); __builtin_amdgcn_s_setprio(0); } while (0)
; #define G8_BAR __builtin_amdgcn_s_barrier()
; template <bool OUTP>
; __device__ __forceinline__ void gemm_phase(const Params& p, int l, char* smem, int vb, int nvb, int pm0, int M, bool fuse, int oz) {
;     ...
;             G8_BAR; G8_WAIT_L(0); G8_MMA(0, 1, At, B1); G8_BAR;
;             G8_LDA(At, 1, 1); G8_STAGE(G8_SA(1, 0), a3, voffA);
;             G8_BAR; G8_WAIT_L(0); G8_MMA(1, 0, At, B0); G8_BAR; G8_SCHED;
;             G8_STAGE(G8_SB(1, 1), b3 + hstepB, voffB);
;             G8_WAIT_V(6); G8_BAR; G8_MMA(1, 1, At, B1); G8_BAR;
;         }
;         if (!(OUTP && fuse)) {
;             const int row0 = cur.pm * BM + wr * 64 + fr, col0 = cur.pn * BM + wc * 32 + 8 * fq;
; #pragma unroll
;             for (int ai = 0; ai < 2; ++ai)
; #pragma unroll
;                 for (int m = 0; m < 4; ++m) {
;                     bf16_t* rowp = Cptr + (size_t)(row0 + ai * HALF + m * 16) * ldc + col0;
; #pragma unroll
;                     for (int bj = 0; bj < 2; ++bj) {
;                         if (col0 + bj * HALF < N) {
;                             const f32x4 v0 = acc[ai][bj][m][0], v1 = acc[ai][bj][m][1];
;                             u32x4 w = {cvt_pk(v0[0], v0[1]), cvt_pk(v0[2], v0[3]), cvt_pk(v1[0], v1[1]), cvt_pk(v1[2], v1[3])};
;                             if (OUTP) {
;                                 __builtin_amdgcn_raw_buffer_store_b128(w, crsrc, (int)(((size_t)(row0 + ai * HALF + m * 16) * ldc + col0 + bj * HALF) * 2), 0, 16);
;                             } else *(u32x4*)(rowp + bj * HALF) = w;
	s_waitcnt lgkmcnt(0)
	s_setprio 1
	s_waitcnt lgkmcnt(0)
	v_mfma_f32_16x16x32_bf16 v[116:119], v[202:205], v[164:167], v[116:119]
	v_mfma_f32_16x16x32_bf16 v[108:111], v[210:213], v[164:167], v[108:111]
	v_mfma_f32_16x16x32_bf16 v[100:103], v[202:205], v[172:175], v[100:103]
	v_mfma_f32_16x16x32_bf16 v[92:95], v[210:213], v[172:175], v[92:95]
	v_mfma_f32_16x16x32_bf16 v[84:87], v[202:205], v[180:183], v[84:87]
	v_mfma_f32_16x16x32_bf16 v[76:79], v[210:213], v[180:183], v[76:79]
	v_mfma_f32_16x16x32_bf16 v[72:75], v[202:205], v[188:191], v[72:75]
	v_mfma_f32_16x16x32_bf16 v[68:71], v[210:213], v[188:191], v[68:71]
	s_mov_b32 m0, s31
	v_lshl_add_u64 v[146:147], v[220:221], 0, s[90:91]
	v_mfma_f32_16x16x32_bf16 v[116:119], v[206:209], v[168:171], v[116:119]
	v_mfma_f32_16x16x32_bf16 v[108:111], v[214:217], v[168:171], v[108:111]
	v_mfma_f32_16x16x32_bf16 v[100:103], v[206:209], v[176:179], v[100:103]
	v_mfma_f32_16x16x32_bf16 v[92:95], v[214:217], v[176:179], v[92:95]
	v_mfma_f32_16x16x32_bf16 v[84:87], v[206:209], v[184:187], v[84:87]
	v_mfma_f32_16x16x32_bf16 v[76:79], v[214:217], v[184:187], v[76:79]
	v_mfma_f32_16x16x32_bf16 v[72:75], v[206:209], v[192:195], v[72:75]
	v_mfma_f32_16x16x32_bf16 v[68:71], v[214:217], v[192:195], v[68:71]
	s_setprio 0
	s_barrier
	ds_read_b128 v[164:167], v150 offset:49152
	ds_read_b128 v[168:171], v150 offset:50176
	ds_read_b128 v[172:175], v150 offset:51200
	ds_read_b128 v[176:179], v150 offset:52224
	ds_read_b128 v[180:183], v150 offset:53248
	ds_read_b128 v[184:187], v150 offset:54272
	ds_read_b128 v[188:191], v150 offset:55296
	ds_read_b128 v[192:195], v150 offset:56320
	global_load_lds_dwordx4 v[146:147], off
	v_lshl_add_u64 v[146:147], v[222:223], 0, s[90:91]
	s_mov_b32 m0, s50
	s_nop 0
	global_load_lds_dwordx4 v[146:147], off
	s_barrier
	s_waitcnt lgkmcnt(0)
	s_setprio 1
	s_waitcnt lgkmcnt(0)
	v_mfma_f32_16x16x32_bf16 v[64:67], v[142:145], v[164:167], v[64:67]
	v_mfma_f32_16x16x32_bf16 v[60:63], v[156:159], v[164:167], v[60:63]
	v_mfma_f32_16x16x32_bf16 v[56:59], v[142:145], v[172:175], v[56:59]
	v_mfma_f32_16x16x32_bf16 v[48:51], v[156:159], v[172:175], v[48:51]
	v_mfma_f32_16x16x32_bf16 v[40:43], v[142:145], v[180:183], v[40:43]
	v_mfma_f32_16x16x32_bf16 v[32:35], v[156:159], v[180:183], v[32:35]
	v_mfma_f32_16x16x32_bf16 v[24:27], v[142:145], v[188:191], v[24:27]
	v_mfma_f32_16x16x32_bf16 v[16:19], v[156:159], v[188:191], v[16:19]
	v_mfma_f32_16x16x32_bf16 v[64:67], v[152:155], v[168:171], v[64:67]
	v_mfma_f32_16x16x32_bf16 v[60:63], v[160:163], v[168:171], v[60:63]
	v_mfma_f32_16x16x32_bf16 v[56:59], v[152:155], v[176:179], v[56:59]
	v_mfma_f32_16x16x32_bf16 v[48:51], v[160:163], v[176:179], v[48:51]
	v_mfma_f32_16x16x32_bf16 v[40:43], v[152:155], v[184:187], v[40:43]
	v_mfma_f32_16x16x32_bf16 v[32:35], v[160:163], v[184:187], v[32:35]
	v_mfma_f32_16x16x32_bf16 v[24:27], v[152:155], v[192:195], v[24:27]
	v_mfma_f32_16x16x32_bf16 v[16:19], v[160:163], v[192:195], v[16:19]
	s_setprio 0
	s_barrier
	s_add_u32 s46, s46, 0x40080
	s_addc_u32 s47, s47, 0
	s_add_i32 s48, s48, s3
	v_lshl_add_u64 v[142:143], s[46:47], 0, v[2:3]
	s_mov_b32 m0, s48
	s_nop 0
	global_load_lds_dwordx4 v[142:143], off
	v_lshl_add_u64 v[142:143], s[46:47], 0, v[136:137]
	s_add_i32 m0, s48, 0x2000
	s_nop 0
	global_load_lds_dwordx4 v[142:143], off
	s_waitcnt vmcnt(8)
	s_barrier
	s_setprio 1
	v_mfma_f32_16x16x32_bf16 v[52:55], v[202:205], v[164:167], v[52:55]
	v_mfma_f32_16x16x32_bf16 v[44:47], v[210:213], v[164:167], v[44:47]
	v_mfma_f32_16x16x32_bf16 v[36:39], v[202:205], v[172:175], v[36:39]
	v_mfma_f32_16x16x32_bf16 v[28:31], v[210:213], v[172:175], v[28:31]
	v_mfma_f32_16x16x32_bf16 v[20:23], v[202:205], v[180:183], v[20:23]
	v_mfma_f32_16x16x32_bf16 v[12:15], v[210:213], v[180:183], v[12:15]
	v_mfma_f32_16x16x32_bf16 v[8:11], v[202:205], v[188:191], v[8:11]
	v_mfma_f32_16x16x32_bf16 v[4:7], v[210:213], v[188:191], v[4:7]
	s_add_i32 s55, s55, 2
	s_add_u32 s38, s38, 0x100
	s_addc_u32 s39, s39, 0
	s_add_u32 s53, s53, 0x100
	s_addc_u32 s54, s54, 0
	s_cmp_gt_u32 s55, 13
	v_mfma_f32_16x16x32_bf16 v[52:55], v[206:209], v[168:171], v[52:55]
	v_mfma_f32_16x16x32_bf16 v[44:47], v[214:217], v[168:171], v[44:47]
	v_mfma_f32_16x16x32_bf16 v[36:39], v[206:209], v[176:179], v[36:39]
	v_mfma_f32_16x16x32_bf16 v[28:31], v[214:217], v[176:179], v[28:31]
	v_mfma_f32_16x16x32_bf16 v[20:23], v[206:209], v[184:187], v[20:23]
	v_mfma_f32_16x16x32_bf16 v[12:15], v[214:217], v[184:187], v[12:15]
	v_mfma_f32_16x16x32_bf16 v[8:11], v[206:209], v[192:195], v[8:11]
	v_mfma_f32_16x16x32_bf16 v[4:7], v[214:217], v[192:195], v[4:7]
	s_setprio 0
	s_barrier
	s_cbranch_scc0 .LBB0_746
	v_lshl_or_b32 v146, s20, 8, v149
	v_ashrrev_i32_e32 v147, 31, v146
	v_lshl_add_u32 v151, s0, 8, v1
	v_lshl_add_u64 v[142:143], v[146:147], 1, s[34:35]
	v_mad_i64_i32 v[144:145], s[0:1], v151, s92, v[142:143]
	s_movk_i32 s0, 0xd10
	s_nop 0
	v_cmp_gt_i32_e32 vcc, s0, v146
	s_and_saveexec_b64 s[0:1], vcc
	s_cbranch_execz .LBB0_749
	v_cvt_pk_bf16_f32 v128, v128, v129
	v_cvt_pk_bf16_f32 v129, v130, v131
	v_cvt_pk_bf16_f32 v130, v124, v125
	v_cvt_pk_bf16_f32 v131, v126, v127
	global_store_dwordx4 v[144:145], v[128:131], off
